# stack6: stack5 + out-projection A-tile staging requests both trips' loads together
# speedup vs baseline: 1.0068x; 1.0010x over previous
; DEVINL unsigned pk2(float lo, float hi) { const f32x2 v = {lo, hi}; return __builtin_bit_cast(unsigned, __builtin_convertvector(v, bf16v2)); }
; DEVINL float bflo(unsigned u) { return __uint_as_float(u << 16); }
; DEVINL float bfhi(unsigned u) { return __uint_as_float(u & 0xffff0000u); }
; DEVINL void phase4(const Params& P, unsigned char* smem) {
;     ...
;         {
;             const int row = t >> 3;
;             const float* sp = SSQ + (size_t)(m0 + row) * 16;
;             const f32x4 a = *(const f32x4*)sp, b2 = *(const f32x4*)(sp + 4), c2 = *(const f32x4*)(sp + 8), d2 = *(const f32x4*)(sp + 12);
;             const float rna = rsqrtf((a.x + a.y + a.z + a.w + b2.x + b2.y + b2.z + b2.w) * (1.f / 512.f) + EPS);
;             const float rsw = rsqrtf((c2.x + c2.y + c2.z + c2.w + d2.x + d2.y + d2.z + d2.w) * (1.f / 512.f) + EPS);
;             const bf16_t* src = ATT + (size_t)(m0 + row) * DM;
; #pragma unroll 8
;             for (int i = 0; i < 16; ++i) {
;                 const int c = (t & 7) + 8 * i;
;                 u32x4 v = *(const u32x4*)(src + c * 8);
;                 const float sc = (c < 64) ? rna : rsw;
;                 v.x = pk2(bflo(v.x) * sc, bfhi(v.x) * sc); v.y = pk2(bflo(v.y) * sc, bfhi(v.y) * sc);
;                 v.z = pk2(bflo(v.z) * sc, bfhi(v.z) * sc); v.w = pk2(bflo(v.w) * sc, bfhi(v.w) * sc);
;                 *(u32x4*)(smem + row * 2048 + ((c ^ (row & 15)) << 4)) = v;
;             }
.LBB0_583:
	global_load_dwordx4 v[2:5], v[10:11], off offset:-896
	global_load_dwordx4 v[6:9], v[10:11], off offset:-768
	global_load_dwordx4 v[14:17], v[10:11], off offset:-640
	global_load_dwordx4 v[18:21], v[10:11], off offset:-512
	global_load_dwordx4 v[22:25], v[10:11], off offset:-384
	global_load_dwordx4 v[26:29], v[10:11], off offset:-256
	global_load_dwordx4 v[30:33], v[10:11], off offset:-128
	global_load_dwordx4 v[34:37], v[10:11], off
	global_load_dwordx4 v[130:133], v[10:11], off offset:128
	global_load_dwordx4 v[134:137], v[10:11], off offset:256
	global_load_dwordx4 v[138:141], v[10:11], off offset:384
	global_load_dwordx4 v[142:145], v[10:11], off offset:512
	global_load_dwordx4 v[146:149], v[10:11], off offset:640
	global_load_dwordx4 v[150:153], v[10:11], off offset:768
	global_load_dwordx4 v[154:157], v[10:11], off offset:896
	global_load_dwordx4 v[158:161], v[10:11], off offset:1024
	v_add_u32_e32 v39, s0, v218
	s_cmp_eq_u32 s0, 0
	v_xor_b32_e32 v40, v39, v220
	v_add_u32_e32 v41, 8, v39
	v_add_u32_e32 v42, 16, v39
	v_add_u32_e32 v43, 24, v39
	v_add_u32_e32 v44, 32, v39
	s_cselect_b64 vcc, -1, 0
	v_add_u32_e32 v45, 40, v39
	v_add_u32_e32 v46, 48, v39
	v_add_u32_e32 v39, 56, v39
	v_lshl_add_u32 v102, v40, 4, v219
	v_xor_b32_e32 v40, v41, v220
	v_xor_b32_e32 v41, v42, v220
	v_xor_b32_e32 v42, v43, v220
	v_xor_b32_e32 v43, v44, v220
	v_cndmask_b32_e32 v38, v13, v12, vcc
	v_xor_b32_e32 v44, v45, v220
	v_xor_b32_e32 v45, v46, v220
	v_xor_b32_e32 v39, v39, v220
	v_lshl_add_u32 v103, v40, 4, v219
	v_lshl_add_u32 v104, v41, 4, v219
	v_lshl_add_u32 v105, v42, 4, v219
	v_lshl_add_u32 v106, v43, 4, v219
	s_add_i32 s0, s0, 64
	v_lshl_add_u32 v107, v44, 4, v219
	v_lshl_add_u32 v108, v45, 4, v219
	v_lshl_add_u64 v[10:11], v[10:11], 0, s[58:59]
	s_cmpk_eq_i32 s0, 0x80
	v_lshl_add_u32 v109, v39, 4, v219
	s_waitcnt vmcnt(15)
	v_lshlrev_b32_e32 v40, 16, v2
	v_and_b32_e32 v41, 0xffff0000, v2
	v_lshlrev_b32_e32 v2, 16, v3
	v_and_b32_e32 v3, 0xffff0000, v3
	v_lshlrev_b32_e32 v42, 16, v4
	v_and_b32_e32 v43, 0xffff0000, v4
	v_lshlrev_b32_e32 v4, 16, v5
	v_and_b32_e32 v5, 0xffff0000, v5
	s_waitcnt vmcnt(14)
	v_lshlrev_b32_e32 v44, 16, v6
	v_and_b32_e32 v45, 0xffff0000, v6
	v_lshlrev_b32_e32 v6, 16, v7
	v_and_b32_e32 v7, 0xffff0000, v7
	v_lshlrev_b32_e32 v46, 16, v8
	v_and_b32_e32 v47, 0xffff0000, v8
	v_lshlrev_b32_e32 v8, 16, v9
	v_and_b32_e32 v9, 0xffff0000, v9
	s_waitcnt vmcnt(13)
	v_lshlrev_b32_e32 v48, 16, v14
	v_and_b32_e32 v49, 0xffff0000, v14
	v_lshlrev_b32_e32 v14, 16, v15
	v_and_b32_e32 v15, 0xffff0000, v15
	v_lshlrev_b32_e32 v50, 16, v16
	v_and_b32_e32 v51, 0xffff0000, v16
	v_lshlrev_b32_e32 v16, 16, v17
	v_and_b32_e32 v17, 0xffff0000, v17
	s_waitcnt vmcnt(12)
	v_lshlrev_b32_e32 v52, 16, v18
	v_and_b32_e32 v53, 0xffff0000, v18
	v_lshlrev_b32_e32 v18, 16, v19
	v_and_b32_e32 v19, 0xffff0000, v19
	v_lshlrev_b32_e32 v54, 16, v20
	v_and_b32_e32 v55, 0xffff0000, v20
	v_lshlrev_b32_e32 v20, 16, v21
	v_and_b32_e32 v21, 0xffff0000, v21
	s_waitcnt vmcnt(11)
	v_lshlrev_b32_e32 v56, 16, v22
	v_and_b32_e32 v57, 0xffff0000, v22
	v_lshlrev_b32_e32 v22, 16, v23
	v_and_b32_e32 v23, 0xffff0000, v23
	v_lshlrev_b32_e32 v58, 16, v24
	v_and_b32_e32 v59, 0xffff0000, v24
	v_lshlrev_b32_e32 v24, 16, v25
	v_and_b32_e32 v25, 0xffff0000, v25
	s_waitcnt vmcnt(10)
	v_lshlrev_b32_e32 v60, 16, v26
	v_and_b32_e32 v61, 0xffff0000, v26
	v_lshlrev_b32_e32 v26, 16, v27
	v_and_b32_e32 v27, 0xffff0000, v27
	v_lshlrev_b32_e32 v62, 16, v28
	v_and_b32_e32 v63, 0xffff0000, v28
	v_lshlrev_b32_e32 v28, 16, v29
	v_and_b32_e32 v29, 0xffff0000, v29
	s_waitcnt vmcnt(9)
	v_lshlrev_b32_e32 v64, 16, v30
	v_and_b32_e32 v65, 0xffff0000, v30
	v_lshlrev_b32_e32 v30, 16, v31
	v_and_b32_e32 v31, 0xffff0000, v31
	v_lshlrev_b32_e32 v66, 16, v32
	v_and_b32_e32 v67, 0xffff0000, v32
	v_lshlrev_b32_e32 v32, 16, v33
	v_and_b32_e32 v33, 0xffff0000, v33
	s_waitcnt vmcnt(8)
	v_lshlrev_b32_e32 v68, 16, v34
	v_and_b32_e32 v69, 0xffff0000, v34
	v_lshlrev_b32_e32 v34, 16, v35
	v_and_b32_e32 v35, 0xffff0000, v35
	v_lshlrev_b32_e32 v70, 16, v36
	v_and_b32_e32 v71, 0xffff0000, v36
	v_lshlrev_b32_e32 v36, 16, v37
	v_and_b32_e32 v37, 0xffff0000, v37
	v_pk_mul_f32 v[40:41], v[38:39], v[40:41] op_sel_hi:[0,1]
	v_pk_mul_f32 v[72:73], v[38:39], v[2:3] op_sel_hi:[0,1]
	v_pk_mul_f32 v[42:43], v[38:39], v[42:43] op_sel_hi:[0,1]
	v_pk_mul_f32 v[74:75], v[38:39], v[4:5] op_sel_hi:[0,1]
	v_pk_mul_f32 v[44:45], v[38:39], v[44:45] op_sel_hi:[0,1]
	v_pk_mul_f32 v[76:77], v[38:39], v[6:7] op_sel_hi:[0,1]
	v_pk_mul_f32 v[46:47], v[38:39], v[46:47] op_sel_hi:[0,1]
	v_pk_mul_f32 v[78:79], v[38:39], v[8:9] op_sel_hi:[0,1]
	v_pk_mul_f32 v[48:49], v[38:39], v[48:49] op_sel_hi:[0,1]
	v_pk_mul_f32 v[80:81], v[38:39], v[14:15] op_sel_hi:[0,1]
	v_pk_mul_f32 v[50:51], v[38:39], v[50:51] op_sel_hi:[0,1]
	v_pk_mul_f32 v[82:83], v[38:39], v[16:17] op_sel_hi:[0,1]
	v_pk_mul_f32 v[52:53], v[38:39], v[52:53] op_sel_hi:[0,1]
	v_pk_mul_f32 v[84:85], v[38:39], v[18:19] op_sel_hi:[0,1]
	v_pk_mul_f32 v[54:55], v[38:39], v[54:55] op_sel_hi:[0,1]
	v_pk_mul_f32 v[86:87], v[38:39], v[20:21] op_sel_hi:[0,1]
	v_pk_mul_f32 v[56:57], v[38:39], v[56:57] op_sel_hi:[0,1]
	v_pk_mul_f32 v[88:89], v[38:39], v[22:23] op_sel_hi:[0,1]
	v_pk_mul_f32 v[58:59], v[38:39], v[58:59] op_sel_hi:[0,1]
	v_pk_mul_f32 v[90:91], v[38:39], v[24:25] op_sel_hi:[0,1]
	v_pk_mul_f32 v[60:61], v[38:39], v[60:61] op_sel_hi:[0,1]
	v_pk_mul_f32 v[92:93], v[38:39], v[26:27] op_sel_hi:[0,1]
	v_pk_mul_f32 v[62:63], v[38:39], v[62:63] op_sel_hi:[0,1]
	v_pk_mul_f32 v[94:95], v[38:39], v[28:29] op_sel_hi:[0,1]
	v_pk_mul_f32 v[64:65], v[38:39], v[64:65] op_sel_hi:[0,1]
; DEVINL unsigned pk2(float lo, float hi) { const f32x2 v = {lo, hi}; return __builtin_bit_cast(unsigned, __builtin_convertvector(v, bf16v2)); }
; DEVINL float bflo(unsigned u) { return __uint_as_float(u << 16); }
; DEVINL float bfhi(unsigned u) { return __uint_as_float(u & 0xffff0000u); }
; DEVINL void phase4(const Params& P, unsigned char* smem) {
;     ...
;             const bf16_t* src = ATT + (size_t)(m0 + row) * DM;
; #pragma unroll 8
;             for (int i = 0; i < 16; ++i) {
;                 const int c = (t & 7) + 8 * i;
;                 u32x4 v = *(const u32x4*)(src + c * 8);
;                 const float sc = (c < 64) ? rna : rsw;
;                 v.x = pk2(bflo(v.x) * sc, bfhi(v.x) * sc); v.y = pk2(bflo(v.y) * sc, bfhi(v.y) * sc);
;                 v.z = pk2(bflo(v.z) * sc, bfhi(v.z) * sc); v.w = pk2(bflo(v.w) * sc, bfhi(v.w) * sc);
;                 *(u32x4*)(smem + row * 2048 + ((c ^ (row & 15)) << 4)) = v;
;             }
	v_pk_mul_f32 v[96:97], v[38:39], v[30:31] op_sel_hi:[0,1]
	v_pk_mul_f32 v[66:67], v[38:39], v[66:67] op_sel_hi:[0,1]
	v_pk_mul_f32 v[98:99], v[38:39], v[32:33] op_sel_hi:[0,1]
	v_pk_mul_f32 v[68:69], v[38:39], v[68:69] op_sel_hi:[0,1]
	v_pk_mul_f32 v[100:101], v[38:39], v[34:35] op_sel_hi:[0,1]
	v_pk_mul_f32 v[70:71], v[38:39], v[70:71] op_sel_hi:[0,1]
	v_pk_mul_f32 v[38:39], v[38:39], v[36:37] op_sel_hi:[0,1]
	v_cvt_pk_bf16_f32 v2, v40, v41
	v_cvt_pk_bf16_f32 v3, v72, v73
	v_cvt_pk_bf16_f32 v4, v42, v43
	v_cvt_pk_bf16_f32 v5, v74, v75
	v_cvt_pk_bf16_f32 v6, v44, v45
	v_cvt_pk_bf16_f32 v7, v76, v77
	v_cvt_pk_bf16_f32 v8, v46, v47
	v_cvt_pk_bf16_f32 v9, v78, v79
	v_cvt_pk_bf16_f32 v14, v48, v49
	v_cvt_pk_bf16_f32 v15, v80, v81
	v_cvt_pk_bf16_f32 v16, v50, v51
	v_cvt_pk_bf16_f32 v17, v82, v83
	v_cvt_pk_bf16_f32 v18, v52, v53
	v_cvt_pk_bf16_f32 v19, v84, v85
	v_cvt_pk_bf16_f32 v20, v54, v55
	v_cvt_pk_bf16_f32 v21, v86, v87
	v_cvt_pk_bf16_f32 v22, v56, v57
	v_cvt_pk_bf16_f32 v23, v88, v89
	v_cvt_pk_bf16_f32 v24, v58, v59
	v_cvt_pk_bf16_f32 v25, v90, v91
	v_cvt_pk_bf16_f32 v26, v60, v61
	v_cvt_pk_bf16_f32 v27, v92, v93
	v_cvt_pk_bf16_f32 v28, v62, v63
	v_cvt_pk_bf16_f32 v29, v94, v95
	v_cvt_pk_bf16_f32 v30, v64, v65
	v_cvt_pk_bf16_f32 v31, v96, v97
	v_cvt_pk_bf16_f32 v32, v66, v67
	v_cvt_pk_bf16_f32 v33, v98, v99
	v_cvt_pk_bf16_f32 v34, v68, v69
	v_cvt_pk_bf16_f32 v35, v100, v101
	v_cvt_pk_bf16_f32 v36, v70, v71
	v_cvt_pk_bf16_f32 v37, v38, v39
	ds_write_b128 v102, v[2:5]
	ds_write_b128 v103, v[6:9]
	ds_write_b128 v104, v[14:17]
	ds_write_b128 v105, v[18:21]
	ds_write_b128 v106, v[22:25]
	ds_write_b128 v107, v[26:29]
	ds_write_b128 v108, v[30:33]
	ds_write_b128 v109, v[34:37]
	s_waitcnt vmcnt(0)
	v_mov_b32_e32 v2, v130
	v_mov_b32_e32 v3, v131
	v_mov_b32_e32 v4, v132
	v_mov_b32_e32 v5, v133
	v_mov_b32_e32 v6, v134
	v_mov_b32_e32 v7, v135
	v_mov_b32_e32 v8, v136
	v_mov_b32_e32 v9, v137
	v_mov_b32_e32 v14, v138
	v_mov_b32_e32 v15, v139
	v_mov_b32_e32 v16, v140
	v_mov_b32_e32 v17, v141
	v_mov_b32_e32 v18, v142
	v_mov_b32_e32 v19, v143
	v_mov_b32_e32 v20, v144
	v_mov_b32_e32 v21, v145
	v_mov_b32_e32 v22, v146
	v_mov_b32_e32 v23, v147
	v_mov_b32_e32 v24, v148
	v_mov_b32_e32 v25, v149
	v_mov_b32_e32 v26, v150
	v_mov_b32_e32 v27, v151
	v_mov_b32_e32 v28, v152
	v_mov_b32_e32 v29, v153
	v_mov_b32_e32 v30, v154
	v_mov_b32_e32 v31, v155
	v_mov_b32_e32 v32, v156
	v_mov_b32_e32 v33, v157
	v_mov_b32_e32 v34, v158
	v_mov_b32_e32 v35, v159
	v_mov_b32_e32 v36, v160
	v_mov_b32_e32 v37, v161
	v_add_u32_e32 v39, s0, v218
	s_cmp_eq_u32 s0, 0
	v_xor_b32_e32 v40, v39, v220
	v_add_u32_e32 v41, 8, v39
	v_add_u32_e32 v42, 16, v39
	v_add_u32_e32 v43, 24, v39
	v_add_u32_e32 v44, 32, v39
	s_cselect_b64 vcc, -1, 0
	v_add_u32_e32 v45, 40, v39
	v_add_u32_e32 v46, 48, v39
	v_add_u32_e32 v39, 56, v39
	v_lshl_add_u32 v102, v40, 4, v219
	v_xor_b32_e32 v40, v41, v220
	v_xor_b32_e32 v41, v42, v220
	v_xor_b32_e32 v42, v43, v220
	v_xor_b32_e32 v43, v44, v220
	v_cndmask_b32_e32 v38, v13, v12, vcc
	v_xor_b32_e32 v44, v45, v220
	v_xor_b32_e32 v45, v46, v220
	v_xor_b32_e32 v39, v39, v220
	v_lshl_add_u32 v103, v40, 4, v219
	v_lshl_add_u32 v104, v41, 4, v219
	v_lshl_add_u32 v105, v42, 4, v219
	v_lshl_add_u32 v106, v43, 4, v219
	s_add_i32 s0, s0, 64
	v_lshl_add_u32 v107, v44, 4, v219
	v_lshl_add_u32 v108, v45, 4, v219
	v_lshl_add_u64 v[10:11], v[10:11], 0, s[58:59]
	s_cmpk_eq_i32 s0, 0x80
	v_lshl_add_u32 v109, v39, 4, v219
	v_lshlrev_b32_e32 v40, 16, v2
	v_and_b32_e32 v41, 0xffff0000, v2
	v_lshlrev_b32_e32 v2, 16, v3
	v_and_b32_e32 v3, 0xffff0000, v3
	v_lshlrev_b32_e32 v42, 16, v4
	v_and_b32_e32 v43, 0xffff0000, v4
	v_lshlrev_b32_e32 v4, 16, v5
	v_and_b32_e32 v5, 0xffff0000, v5
	v_lshlrev_b32_e32 v44, 16, v6
	v_and_b32_e32 v45, 0xffff0000, v6
	v_lshlrev_b32_e32 v6, 16, v7
	v_and_b32_e32 v7, 0xffff0000, v7
	v_lshlrev_b32_e32 v46, 16, v8
	v_and_b32_e32 v47, 0xffff0000, v8
	v_lshlrev_b32_e32 v8, 16, v9
	v_and_b32_e32 v9, 0xffff0000, v9
	v_lshlrev_b32_e32 v48, 16, v14
	v_and_b32_e32 v49, 0xffff0000, v14
	v_lshlrev_b32_e32 v14, 16, v15
	v_and_b32_e32 v15, 0xffff0000, v15
	v_lshlrev_b32_e32 v50, 16, v16
	v_and_b32_e32 v51, 0xffff0000, v16
	v_lshlrev_b32_e32 v16, 16, v17
	v_and_b32_e32 v17, 0xffff0000, v17
	v_lshlrev_b32_e32 v52, 16, v18
	v_and_b32_e32 v53, 0xffff0000, v18
	v_lshlrev_b32_e32 v18, 16, v19
	v_and_b32_e32 v19, 0xffff0000, v19
	v_lshlrev_b32_e32 v54, 16, v20
	v_and_b32_e32 v55, 0xffff0000, v20
	v_lshlrev_b32_e32 v20, 16, v21
	v_and_b32_e32 v21, 0xffff0000, v21
	v_lshlrev_b32_e32 v56, 16, v22
	v_and_b32_e32 v57, 0xffff0000, v22
	v_lshlrev_b32_e32 v22, 16, v23
	v_and_b32_e32 v23, 0xffff0000, v23
	v_lshlrev_b32_e32 v58, 16, v24
	v_and_b32_e32 v59, 0xffff0000, v24
	v_lshlrev_b32_e32 v24, 16, v25
	v_and_b32_e32 v25, 0xffff0000, v25
	v_lshlrev_b32_e32 v60, 16, v26
	v_and_b32_e32 v61, 0xffff0000, v26
	v_lshlrev_b32_e32 v26, 16, v27
	v_and_b32_e32 v27, 0xffff0000, v27
	v_lshlrev_b32_e32 v62, 16, v28
	v_and_b32_e32 v63, 0xffff0000, v28
	v_lshlrev_b32_e32 v28, 16, v29
	v_and_b32_e32 v29, 0xffff0000, v29
	v_lshlrev_b32_e32 v64, 16, v30
	v_and_b32_e32 v65, 0xffff0000, v30
	v_lshlrev_b32_e32 v30, 16, v31
	v_and_b32_e32 v31, 0xffff0000, v31
	v_lshlrev_b32_e32 v66, 16, v32
	v_and_b32_e32 v67, 0xffff0000, v32
	v_lshlrev_b32_e32 v32, 16, v33
	v_and_b32_e32 v33, 0xffff0000, v33
	v_lshlrev_b32_e32 v68, 16, v34
	v_and_b32_e32 v69, 0xffff0000, v34
	v_lshlrev_b32_e32 v34, 16, v35
	v_and_b32_e32 v35, 0xffff0000, v35
	v_lshlrev_b32_e32 v70, 16, v36
	v_and_b32_e32 v71, 0xffff0000, v36
	v_lshlrev_b32_e32 v36, 16, v37
	v_and_b32_e32 v37, 0xffff0000, v37
	v_pk_mul_f32 v[40:41], v[38:39], v[40:41] op_sel_hi:[0,1]
; DEVINL unsigned pk2(float lo, float hi) { const f32x2 v = {lo, hi}; return __builtin_bit_cast(unsigned, __builtin_convertvector(v, bf16v2)); }
; DEVINL float bflo(unsigned u) { return __uint_as_float(u << 16); }
; DEVINL float bfhi(unsigned u) { return __uint_as_float(u & 0xffff0000u); }
; DEVINL void phase4(const Params& P, unsigned char* smem) {
;     ...
;             for (int i = 0; i < 16; ++i) {
;                 const int c = (t & 7) + 8 * i;
;                 u32x4 v = *(const u32x4*)(src + c * 8);
;                 const float sc = (c < 64) ? rna : rsw;
;                 v.x = pk2(bflo(v.x) * sc, bfhi(v.x) * sc); v.y = pk2(bflo(v.y) * sc, bfhi(v.y) * sc);
;                 v.z = pk2(bflo(v.z) * sc, bfhi(v.z) * sc); v.w = pk2(bflo(v.w) * sc, bfhi(v.w) * sc);
;                 *(u32x4*)(smem + row * 2048 + ((c ^ (row & 15)) << 4)) = v;
;             }
;         }
;         __syncthreads();
;         f32x4 acc[8][4];
; #pragma unroll
;         for (int i = 0; i < 8; ++i)
; #pragma unroll
;             for (int mi = 0; mi < 4; ++mi) acc[i][mi] = (f32x4){0.f, 0.f, 0.f, 0.f};
	v_pk_mul_f32 v[72:73], v[38:39], v[2:3] op_sel_hi:[0,1]
	v_pk_mul_f32 v[42:43], v[38:39], v[42:43] op_sel_hi:[0,1]
	v_pk_mul_f32 v[74:75], v[38:39], v[4:5] op_sel_hi:[0,1]
	v_pk_mul_f32 v[44:45], v[38:39], v[44:45] op_sel_hi:[0,1]
	v_pk_mul_f32 v[76:77], v[38:39], v[6:7] op_sel_hi:[0,1]
	v_pk_mul_f32 v[46:47], v[38:39], v[46:47] op_sel_hi:[0,1]
	v_pk_mul_f32 v[78:79], v[38:39], v[8:9] op_sel_hi:[0,1]
	v_pk_mul_f32 v[48:49], v[38:39], v[48:49] op_sel_hi:[0,1]
	v_pk_mul_f32 v[80:81], v[38:39], v[14:15] op_sel_hi:[0,1]
	v_pk_mul_f32 v[50:51], v[38:39], v[50:51] op_sel_hi:[0,1]
	v_pk_mul_f32 v[82:83], v[38:39], v[16:17] op_sel_hi:[0,1]
	v_pk_mul_f32 v[52:53], v[38:39], v[52:53] op_sel_hi:[0,1]
	v_pk_mul_f32 v[84:85], v[38:39], v[18:19] op_sel_hi:[0,1]
	v_pk_mul_f32 v[54:55], v[38:39], v[54:55] op_sel_hi:[0,1]
	v_pk_mul_f32 v[86:87], v[38:39], v[20:21] op_sel_hi:[0,1]
	v_pk_mul_f32 v[56:57], v[38:39], v[56:57] op_sel_hi:[0,1]
	v_pk_mul_f32 v[88:89], v[38:39], v[22:23] op_sel_hi:[0,1]
	v_pk_mul_f32 v[58:59], v[38:39], v[58:59] op_sel_hi:[0,1]
	v_pk_mul_f32 v[90:91], v[38:39], v[24:25] op_sel_hi:[0,1]
	v_pk_mul_f32 v[60:61], v[38:39], v[60:61] op_sel_hi:[0,1]
	v_pk_mul_f32 v[92:93], v[38:39], v[26:27] op_sel_hi:[0,1]
	v_pk_mul_f32 v[62:63], v[38:39], v[62:63] op_sel_hi:[0,1]
	v_pk_mul_f32 v[94:95], v[38:39], v[28:29] op_sel_hi:[0,1]
	v_pk_mul_f32 v[64:65], v[38:39], v[64:65] op_sel_hi:[0,1]
	v_pk_mul_f32 v[96:97], v[38:39], v[30:31] op_sel_hi:[0,1]
	v_pk_mul_f32 v[66:67], v[38:39], v[66:67] op_sel_hi:[0,1]
	v_pk_mul_f32 v[98:99], v[38:39], v[32:33] op_sel_hi:[0,1]
	v_pk_mul_f32 v[68:69], v[38:39], v[68:69] op_sel_hi:[0,1]
	v_pk_mul_f32 v[100:101], v[38:39], v[34:35] op_sel_hi:[0,1]
	v_pk_mul_f32 v[70:71], v[38:39], v[70:71] op_sel_hi:[0,1]
	v_pk_mul_f32 v[38:39], v[38:39], v[36:37] op_sel_hi:[0,1]
	v_cvt_pk_bf16_f32 v2, v40, v41
	v_cvt_pk_bf16_f32 v3, v72, v73
	v_cvt_pk_bf16_f32 v4, v42, v43
	v_cvt_pk_bf16_f32 v5, v74, v75
	v_cvt_pk_bf16_f32 v6, v44, v45
	v_cvt_pk_bf16_f32 v7, v76, v77
	v_cvt_pk_bf16_f32 v8, v46, v47
	v_cvt_pk_bf16_f32 v9, v78, v79
	v_cvt_pk_bf16_f32 v14, v48, v49
	v_cvt_pk_bf16_f32 v15, v80, v81
	v_cvt_pk_bf16_f32 v16, v50, v51
	v_cvt_pk_bf16_f32 v17, v82, v83
	v_cvt_pk_bf16_f32 v18, v52, v53
	v_cvt_pk_bf16_f32 v19, v84, v85
	v_cvt_pk_bf16_f32 v20, v54, v55
	v_cvt_pk_bf16_f32 v21, v86, v87
	v_cvt_pk_bf16_f32 v22, v56, v57
	v_cvt_pk_bf16_f32 v23, v88, v89
	v_cvt_pk_bf16_f32 v24, v58, v59
	v_cvt_pk_bf16_f32 v25, v90, v91
	v_cvt_pk_bf16_f32 v26, v60, v61
	v_cvt_pk_bf16_f32 v27, v92, v93
	v_cvt_pk_bf16_f32 v28, v62, v63
	v_cvt_pk_bf16_f32 v29, v94, v95
	v_cvt_pk_bf16_f32 v30, v64, v65
	v_cvt_pk_bf16_f32 v31, v96, v97
	v_cvt_pk_bf16_f32 v32, v66, v67
	v_cvt_pk_bf16_f32 v33, v98, v99
	v_cvt_pk_bf16_f32 v34, v68, v69
	v_cvt_pk_bf16_f32 v35, v100, v101
	v_cvt_pk_bf16_f32 v36, v70, v71
	v_cvt_pk_bf16_f32 v37, v38, v39
	ds_write_b128 v102, v[2:5]
	ds_write_b128 v103, v[6:9]
	ds_write_b128 v104, v[14:17]
	ds_write_b128 v105, v[18:21]
	ds_write_b128 v106, v[22:25]
	ds_write_b128 v107, v[26:29]
	ds_write_b128 v108, v[30:33]
	ds_write_b128 v109, v[34:37]
	v_mov_b32_e32 v5, 0
	v_and_b32_e32 v238, 15, v190
	v_ashrrev_i32_e32 v204, 4, v190
	s_and_b64 vcc, exec, s[42:43]
	v_mov_b32_e32 v4, v5
	v_mov_b32_e32 v3, v5
	v_mov_b32_e32 v2, v5
	v_mov_b32_e32 v9, v5
	v_mov_b32_e32 v8, v5
	v_mov_b32_e32 v7, v5
	v_mov_b32_e32 v6, v5
	v_mov_b32_e32 v69, v5
	v_mov_b32_e32 v68, v5
	v_mov_b32_e32 v67, v5
	v_mov_b32_e32 v66, v5
	v_mov_b32_e32 v73, v5
	v_mov_b32_e32 v72, v5
	v_mov_b32_e32 v71, v5
	v_mov_b32_e32 v70, v5
	v_mov_b32_e32 v13, v5
	v_mov_b32_e32 v12, v5
	v_mov_b32_e32 v11, v5
	v_mov_b32_e32 v10, v5
	v_mov_b32_e32 v17, v5
	v_mov_b32_e32 v16, v5
	v_mov_b32_e32 v15, v5
	v_mov_b32_e32 v14, v5
	v_mov_b32_e32 v77, v5
	v_mov_b32_e32 v76, v5
	v_mov_b32_e32 v75, v5
	v_mov_b32_e32 v74, v5
	v_mov_b32_e32 v81, v5
	v_mov_b32_e32 v80, v5
	v_mov_b32_e32 v79, v5
	v_mov_b32_e32 v78, v5
	v_mov_b32_e32 v21, v5
	v_mov_b32_e32 v20, v5
	v_mov_b32_e32 v19, v5
	v_mov_b32_e32 v18, v5
	v_mov_b32_e32 v25, v5
	v_mov_b32_e32 v24, v5
	v_mov_b32_e32 v23, v5
	v_mov_b32_e32 v22, v5
	v_mov_b32_e32 v85, v5
	v_mov_b32_e32 v84, v5
	v_mov_b32_e32 v83, v5
	v_mov_b32_e32 v82, v5
	v_mov_b32_e32 v89, v5
	v_mov_b32_e32 v88, v5
	v_mov_b32_e32 v87, v5
	v_mov_b32_e32 v86, v5
	v_mov_b32_e32 v29, v5
	v_mov_b32_e32 v28, v5
	v_mov_b32_e32 v27, v5
	v_mov_b32_e32 v26, v5
	v_mov_b32_e32 v33, v5
	v_mov_b32_e32 v32, v5
	v_mov_b32_e32 v31, v5
	v_mov_b32_e32 v30, v5
	v_mov_b32_e32 v93, v5
	v_mov_b32_e32 v92, v5
	v_mov_b32_e32 v91, v5
	v_mov_b32_e32 v90, v5
	v_mov_b32_e32 v97, v5
	v_mov_b32_e32 v96, v5
	v_mov_b32_e32 v95, v5
	v_mov_b32_e32 v94, v5
	v_mov_b32_e32 v129, v5
	v_mov_b32_e32 v128, v5
	v_mov_b32_e32 v127, v5
	v_mov_b32_e32 v126, v5
	v_mov_b32_e32 v125, v5
	v_mov_b32_e32 v124, v5
	v_mov_b32_e32 v123, v5
	v_mov_b32_e32 v122, v5
	v_mov_b32_e32 v65, v5
	v_mov_b32_e32 v64, v5
	v_mov_b32_e32 v63, v5
	v_mov_b32_e32 v62, v5
	v_mov_b32_e32 v61, v5
	v_mov_b32_e32 v60, v5
	v_mov_b32_e32 v59, v5
	v_mov_b32_e32 v58, v5
	v_mov_b32_e32 v121, v5
	v_mov_b32_e32 v120, v5
	v_mov_b32_e32 v119, v5
	v_mov_b32_e32 v118, v5
	v_mov_b32_e32 v117, v5
	v_mov_b32_e32 v116, v5
	v_mov_b32_e32 v115, v5
	v_mov_b32_e32 v114, v5
	v_mov_b32_e32 v57, v5
	v_mov_b32_e32 v56, v5
	v_mov_b32_e32 v55, v5
	v_mov_b32_e32 v54, v5
	v_mov_b32_e32 v53, v5
	v_mov_b32_e32 v52, v5
	v_mov_b32_e32 v51, v5
	v_mov_b32_e32 v50, v5
	v_mov_b32_e32 v113, v5
	v_mov_b32_e32 v112, v5
	v_mov_b32_e32 v111, v5
	v_mov_b32_e32 v110, v5
	v_mov_b32_e32 v109, v5
	v_mov_b32_e32 v108, v5
	v_mov_b32_e32 v107, v5
	v_mov_b32_e32 v106, v5
	v_mov_b32_e32 v49, v5
	v_mov_b32_e32 v48, v5
	v_mov_b32_e32 v47, v5
	v_mov_b32_e32 v46, v5
	v_mov_b32_e32 v45, v5
	v_mov_b32_e32 v44, v5
	v_mov_b32_e32 v43, v5
	v_mov_b32_e32 v42, v5
	v_mov_b32_e32 v105, v5
	v_mov_b32_e32 v104, v5
	v_mov_b32_e32 v103, v5
	v_mov_b32_e32 v102, v5
	v_mov_b32_e32 v101, v5
	v_mov_b32_e32 v100, v5
	v_mov_b32_e32 v99, v5
	v_mov_b32_e32 v98, v5
	v_mov_b32_e32 v41, v5
	v_mov_b32_e32 v40, v5
	v_mov_b32_e32 v39, v5
	v_mov_b32_e32 v38, v5
	v_mov_b32_e32 v37, v5
	v_mov_b32_e32 v36, v5
	v_mov_b32_e32 v35, v5
	v_mov_b32_e32 v34, v5
	s_waitcnt lgkmcnt(0)
	s_barrier
; #define LOADB(dst, ks_) do { const unsigned char* ub_ = wb + (size_t)((ks_) * 144) * 1024; \
;         _Pragma("unroll") for (int j_ = 0; j_ < 8; ++j_) dst[j_] = *(const bf16x8*)(ub_ + j_ * 1024 + voff); } while (0)
; #define LOADA(fd, ks_) do { _Pragma("unroll") for (int mi_ = 0; mi_ < 4; ++mi_) fd[mi_] = AFRAG(mi_, ks_); } while (0)
; #define LOADB(dst, ks_) do { const unsigned char* ub_ = wb + (size_t)((ks_) * 64) * 1024; \
;         _Pragma("unroll") for (int j_ = 0; j_ < 8; ++j_) dst[j_] = *(const bf16x8*)(ub_ + j_ * 1024 + voff); } while (0)
; #define LOADA(fd, ks_) do { _Pragma("unroll") for (int mi_ = 0; mi_ < 4; ++mi_) fd[mi_] = AFRAG(mi_, ks_); } while (0)
; DEVINL void phase4(const Params& P, unsigned char* smem) {
;     ...
;         if (!SKIPF(32)) {
;             const unsigned char* wb = (const unsigned char*)(P.ws + WS_WOF) + (size_t)(8 * wv) * 1024;
;             unsigned voff = (unsigned)(lane * 16);
;             asm volatile("" : "+v"(voff));
;             const int aoff = lr * 2048;
;     ...
;             bf16x8 b0[8], b1[8];
;     ...
;             bf16x8 fa[4];
;             LOADB(b0, 0); LOADA(fa, 0);
	s_cbranch_vccz .LBB0_587
	v_lshlrev_b32_e32 v178, 4, v190
	global_load_dwordx4 v[130:133], v178, s[44:45]
	global_load_dwordx4 v[134:137], v178, s[44:45] offset:1024
	global_load_dwordx4 v[138:141], v178, s[44:45] offset:2048
	global_load_dwordx4 v[142:145], v178, s[44:45] offset:3072
	v_lshl_add_u64 v[192:193], s[44:45], 0, v[178:179]
	v_add_co_u32_e32 v2, vcc, 0x1000, v192
	v_lshl_add_u32 v191, v238, 11, 0
	s_nop 0
	v_addc_co_u32_e32 v3, vcc, 0, v193, vcc
	global_load_dwordx4 v[158:161], v[2:3], off
	global_load_dwordx4 v[154:157], v[2:3], off offset:1024
	global_load_dwordx4 v[150:153], v[2:3], off offset:2048
	global_load_dwordx4 v[146:149], v[2:3], off offset:3072
	v_xor_b32_e32 v2, v204, v238
	v_lshl_add_u32 v2, v2, 4, v191
	v_add_u32_e32 v3, 0x10000, v2
	ds_read_b128 v[174:177], v2
	ds_read_b128 v[170:173], v2 offset:32768
	v_add_u32_e32 v2, 0x18000, v2
	ds_read_b128 v[166:169], v3
	ds_read_b128 v[162:165], v2
	v_mov_b32_e32 v34, 0
	s_mov_b32 s0, 0
	v_add_u32_e32 v196, 4, v204
	v_lshl_add_u64 v[194:195], s[52:53], 0, v[178:179]
	v_mov_b32_e32 v35, v34
	v_mov_b32_e32 v36, v34
	v_mov_b32_e32 v37, v34
	v_mov_b32_e32 v38, v34
	v_mov_b32_e32 v39, v34
	v_mov_b32_e32 v40, v34
	v_mov_b32_e32 v41, v34
	v_mov_b32_e32 v98, v34
	v_mov_b32_e32 v99, v34
	v_mov_b32_e32 v100, v34
	v_mov_b32_e32 v101, v34
	v_mov_b32_e32 v102, v34
	v_mov_b32_e32 v103, v34
	v_mov_b32_e32 v104, v34
	v_mov_b32_e32 v105, v34
	v_mov_b32_e32 v42, v34
	v_mov_b32_e32 v43, v34
	v_mov_b32_e32 v44, v34
	v_mov_b32_e32 v45, v34
	v_mov_b32_e32 v46, v34
	v_mov_b32_e32 v47, v34
	v_mov_b32_e32 v48, v34
	v_mov_b32_e32 v49, v34
	v_mov_b32_e32 v106, v34
	v_mov_b32_e32 v107, v34
	v_mov_b32_e32 v108, v34
	v_mov_b32_e32 v109, v34
	v_mov_b32_e32 v110, v34
	v_mov_b32_e32 v111, v34
	v_mov_b32_e32 v112, v34
	v_mov_b32_e32 v113, v34
	v_mov_b32_e32 v50, v34
	v_mov_b32_e32 v51, v34
	v_mov_b32_e32 v52, v34
	v_mov_b32_e32 v53, v34
	v_mov_b32_e32 v54, v34
	v_mov_b32_e32 v55, v34
	v_mov_b32_e32 v56, v34
	v_mov_b32_e32 v57, v34
	v_mov_b32_e32 v114, v34
	v_mov_b32_e32 v115, v34
	v_mov_b32_e32 v116, v34
	v_mov_b32_e32 v117, v34
	v_mov_b32_e32 v118, v34
	v_mov_b32_e32 v119, v34
	v_mov_b32_e32 v120, v34
	v_mov_b32_e32 v121, v34
	v_mov_b32_e32 v58, v34
	v_mov_b32_e32 v59, v34
	v_mov_b32_e32 v60, v34
	v_mov_b32_e32 v61, v34
	v_mov_b32_e32 v62, v34
	v_mov_b32_e32 v63, v34
	v_mov_b32_e32 v64, v34
	v_mov_b32_e32 v65, v34
	v_mov_b32_e32 v122, v34
	v_mov_b32_e32 v123, v34
	v_mov_b32_e32 v124, v34
	v_mov_b32_e32 v125, v34
	v_mov_b32_e32 v126, v34
	v_mov_b32_e32 v127, v34
	v_mov_b32_e32 v128, v34
	v_mov_b32_e32 v129, v34
	v_mov_b32_e32 v94, v34
	v_mov_b32_e32 v95, v34
	v_mov_b32_e32 v96, v34
	v_mov_b32_e32 v97, v34
	v_mov_b32_e32 v90, v34
	v_mov_b32_e32 v91, v34
	v_mov_b32_e32 v92, v34
	v_mov_b32_e32 v93, v34
	v_mov_b32_e32 v30, v34
	v_mov_b32_e32 v31, v34
	v_mov_b32_e32 v32, v34
	v_mov_b32_e32 v33, v34
	v_mov_b32_e32 v26, v34
	v_mov_b32_e32 v27, v34
	v_mov_b32_e32 v28, v34
	v_mov_b32_e32 v29, v34
	v_mov_b32_e32 v86, v34
	v_mov_b32_e32 v87, v34
	v_mov_b32_e32 v88, v34
	v_mov_b32_e32 v89, v34
	v_mov_b32_e32 v82, v34
	v_mov_b32_e32 v83, v34
	v_mov_b32_e32 v84, v34
	v_mov_b32_e32 v85, v34
	v_mov_b32_e32 v22, v34
	v_mov_b32_e32 v23, v34
	v_mov_b32_e32 v24, v34
	v_mov_b32_e32 v25, v34
	v_mov_b32_e32 v18, v34
	v_mov_b32_e32 v19, v34
	v_mov_b32_e32 v20, v34
	v_mov_b32_e32 v21, v34
	v_mov_b32_e32 v78, v34
	v_mov_b32_e32 v79, v34
	v_mov_b32_e32 v80, v34
	v_mov_b32_e32 v81, v34
	v_mov_b32_e32 v74, v34
	v_mov_b32_e32 v75, v34
	v_mov_b32_e32 v76, v34
	v_mov_b32_e32 v77, v34
	v_mov_b32_e32 v14, v34
	v_mov_b32_e32 v15, v34
	v_mov_b32_e32 v16, v34
	v_mov_b32_e32 v17, v34
	v_mov_b32_e32 v10, v34
	v_mov_b32_e32 v11, v34
	v_mov_b32_e32 v12, v34
	v_mov_b32_e32 v13, v34
	v_mov_b32_e32 v70, v34
	v_mov_b32_e32 v71, v34
	v_mov_b32_e32 v72, v34
	v_mov_b32_e32 v73, v34
	v_mov_b32_e32 v66, v34
	v_mov_b32_e32 v67, v34
	v_mov_b32_e32 v68, v34
	v_mov_b32_e32 v69, v34
	v_mov_b32_e32 v6, v34
	v_mov_b32_e32 v7, v34
	v_mov_b32_e32 v8, v34
	v_mov_b32_e32 v9, v34
	v_mov_b32_e32 v2, v34
	v_mov_b32_e32 v3, v34
	v_mov_b32_e32 v4, v34
	v_mov_b32_e32 v5, v34
